# W_in GEMM epilogue: bias taken by ds_bpermute from one dword per lane requested in the unit's first k-iteration (no vmcnt(0) drain of the next unit's prefetch)
# baseline (speedup 1.0000x reference)
; #define PG8_STAGE(bufoff, gbase, voff) do { _Pragma("unroll") for (int _i = 0; _i < 2; ++_i) \
;         __builtin_amdgcn_global_load_lds((const unsigned*)((const char*)(gbase) + (voff)[_i]), (LAS unsigned*)(lds + (bufoff) + ldsw + _i * 8192), 16, 0, 0); } while (0)
; #define PG8_LDA(dst, b, h) do { _Pragma("unroll") for (int m = 0; m < 4; ++m) _Pragma("unroll") for (int k = 0; k < 2; ++k) dst[m][k] = *(const LAS bf16x8*)(lds + PG8_SA(b, h) + aoff + m * 2048 + k * 1024); } while (0)
; #define PG8_LDB(dst, b, h) do { _Pragma("unroll") for (int n = 0; n < 2; ++n) _Pragma("unroll") for (int k = 0; k < 2; ++k) dst[n][k] = *(const LAS bf16x8*)(lds + PG8_SB(b, h) + boff + n * 2048 + k * 1024); } while (0)
; #define PG8_MMA(ai, bj, At, Bt) do { __builtin_amdgcn_s_setprio(1); _Pragma("unroll") for (int m = 0; m < 4; ++m) _Pragma("unroll") for (int n = 0; n < 2; ++n) _Pragma("unroll") for (int k = 0; k < 2; ++k) \
;         acc[ai][bj][m][n] = __builtin_amdgcn_mfma_f32_16x16x32_bf16(Bt[n][k], At[m][k], acc[ai][bj][m][n], 0, 0, 0); __builtin_amdgcn_s_setprio(0); } while (0)
; template <class Epi, class Sched, bool ALIGN_EPI = true, bool SP2 = true>
; __device__ __forceinline__ void gemm_phase(LAS unsigned char* lds, const Dims g, const Sched& S, const Epi& E) {
;     ...
;         for (int t = 0; t < nt; t += 2) {
;             const bool last = (t == nt - 2);
;             const char* a1 = cA + (size_t)(t + 1) * kstep;
;             const char* a2 = last ? nA : cA + (size_t)(t + 2) * kstep; const char* b2 = last ? nB : cB + (size_t)(t + 2) * kstep;
;             const char* a3 = a2 + kstep; const char* b3 = b2 + kstep;
;             if constexpr (SP2) {
;             PG8_LDB(B0, 0, 0); PG8_LDB(B1, 0, 1); PG8_SCHED; PG8_LDA(At, 0, 0); PG8_STAGE(PG8_SA(1, 1), a1 + hstepA, voffA);
;             PG8_WAIT_V(8); PG8_WAIT_L(0); PG8_BAR; PG8_MMA(0, 0, At, B0); PG8_MMA(0, 1, At, B1); PG8_BAR; PG8_SCHED;
;     DI void operator()(const f32x4 (&acc)[2][2][4][2], const Unit& u, int wr, int wc, int fr, int fq) const {
;         const int row0 = u.pm * BM + wr * 64 + fr, col0 = u.pn * BM + wc * 32 + 8 * fq;
;         f32x4 bv[2][2];
; #pragma unroll
;         for (int bj = 0; bj < 2; ++bj)
; #pragma unroll
;             for (int n = 0; n < 2; ++n) bv[bj][n] = bias ? *(const f32x4*)(bias + col0 + bj * HALF + 4 * n) : (f32x4){0.f, 0.f, 0.f, 0.f};
.LBB0_326:
	s_cmp_lg_i32 s31, -2
	s_cbranch_scc1 .Lg1b_skip
	v_and_b32_e32 v252, 31, v0
	v_bfe_u32 v253, v0, 5, 1
	v_lshl_or_b32 v252, v253, 7, v252
	v_bfe_u32 v253, v0, 6, 2
	v_lshl_or_b32 v252, v253, 5, v252
	v_lshlrev_b32_e32 v252, 2, v252
	v_bfe_u32 v253, v0, 4, 2
	v_lshlrev_b32_e32 v253, 5, v253
	s_lshl_b32 s80, s60, 10
	s_add_u32 s80, s24, s80
	s_addc_u32 s81, s25, 0
	global_load_dword v233, v252, s[80:81]

; DI unsigned pk2(float a, float b) { f32x2 v = {a, b}; bf16x2_t r = __builtin_convertvector(v, bf16x2_t); return __builtin_bit_cast(unsigned, r); }
;     DI void operator()(const f32x4 (&acc)[2][2][4][2], const Unit& u, int wr, int wc, int fr, int fq) const {
;         const int row0 = u.pm * BM + wr * 64 + fr, col0 = u.pn * BM + wc * 32 + 8 * fq;
;         f32x4 bv[2][2];
; #pragma unroll
;         for (int bj = 0; bj < 2; ++bj)
; #pragma unroll
;             for (int n = 0; n < 2; ++n) bv[bj][n] = bias ? *(const f32x4*)(bias + col0 + bj * HALF + 4 * n) : (f32x4){0.f, 0.f, 0.f, 0.f};
; #pragma unroll
;         for (int ai = 0; ai < 2; ++ai)
; #pragma unroll
;             for (int m = 0; m < 4; ++m) { bf16* rowp = O + (size_t)(row0 + ai * HALF + m * 16) * ldc + col0;
; #pragma unroll
;                 for (int bj = 0; bj < 2; ++bj) { const f32x4 v0 = acc[ai][bj][m][0] + bv[bj][0], v1 = acc[ai][bj][m][1] + bv[bj][1];
;                     u32x4 w; w.x = pk2(v0[0], v0[1]); w.y = pk2(v0[2], v0[3]); w.z = pk2(v1[0], v1[1]); w.w = pk2(v1[2], v1[3]);
;                     *(u32x4*)(rowp + bj * HALF) = w; } }
.LBB0_329:
	v_lshl_or_b32 v160, s60, 8, v172
	v_ashrrev_i32_e32 v161, 31, v160
	ds_bpermute_b32 v136, v253, v233
	ds_bpermute_b32 v137, v253, v233 offset:4
	ds_bpermute_b32 v138, v253, v233 offset:8
	ds_bpermute_b32 v139, v253, v233 offset:12
	ds_bpermute_b32 v132, v253, v233 offset:16
	ds_bpermute_b32 v133, v253, v233 offset:20
	ds_bpermute_b32 v134, v253, v233 offset:24
	ds_bpermute_b32 v135, v253, v233 offset:28
	ds_bpermute_b32 v144, v253, v233 offset:128
	ds_bpermute_b32 v145, v253, v233 offset:132
	ds_bpermute_b32 v146, v253, v233 offset:136
	ds_bpermute_b32 v147, v253, v233 offset:140
	ds_bpermute_b32 v140, v253, v233 offset:144
	ds_bpermute_b32 v141, v253, v233 offset:148
	ds_bpermute_b32 v142, v253, v233 offset:152
	ds_bpermute_b32 v143, v253, v233 offset:156
	v_lshl_add_u32 v174, s42, 8, v162
	v_mov_b64_e32 v[158:159], s[12:13]
	v_mad_i64_i32 v[164:165], s[2:3], v174, s15, v[158:159]
	v_lshlrev_b64 v[160:161], 1, v[160:161]
	s_waitcnt lgkmcnt(0)
	v_pk_add_f32 v[130:131], v[130:131], v[138:139]
	v_pk_add_f32 v[128:129], v[128:129], v[136:137]
	v_pk_add_f32 v[166:167], v[126:127], v[134:135]
	v_pk_add_f32 v[126:127], v[124:125], v[132:133]
	v_lshl_add_u64 v[164:165], v[164:165], 0, v[160:161]
	v_cvt_pk_bf16_f32 v124, v128, v129
	v_cvt_pk_bf16_f32 v125, v130, v131
	v_cvt_pk_bf16_f32 v126, v126, v127
	v_cvt_pk_bf16_f32 v127, v166, v167
	global_store_dwordx4 v[164:165], v[124:127], off
	v_pk_add_f32 v[122:123], v[122:123], v[146:147]
	v_pk_add_f32 v[120:121], v[120:121], v[144:145]
	v_pk_add_f32 v[124:125], v[110:111], v[142:143]
	v_pk_add_f32 v[110:111], v[108:109], v[140:141]
	v_cvt_pk_bf16_f32 v108, v120, v121
	v_cvt_pk_bf16_f32 v109, v122, v123
	v_cvt_pk_bf16_f32 v110, v110, v111
	v_cvt_pk_bf16_f32 v111, v124, v125
	global_store_dwordx4 v[164:165], v[108:111], off offset:256
	v_pk_add_f32 v[114:115], v[114:115], v[134:135]
	v_pk_add_f32 v[112:113], v[112:113], v[132:133]
	v_or_b32_e32 v108, 16, v174
	v_mad_i64_i32 v[108:109], s[2:3], v108, s15, v[158:159]
	v_lshl_add_u64 v[120:121], v[108:109], 0, v[160:161]
	v_pk_add_f32 v[110:111], v[118:119], v[138:139]
	v_pk_add_f32 v[108:109], v[116:117], v[136:137]
	v_pk_add_f32 v[102:103], v[102:103], v[146:147]
	v_cvt_pk_bf16_f32 v108, v108, v109
	v_cvt_pk_bf16_f32 v109, v110, v111
	v_cvt_pk_bf16_f32 v110, v112, v113
	v_cvt_pk_bf16_f32 v111, v114, v115
	global_store_dwordx4 v[120:121], v[108:111], off
	v_pk_add_f32 v[100:101], v[100:101], v[144:145]
	v_pk_add_f32 v[98:99], v[98:99], v[134:135]
	v_pk_add_f32 v[108:109], v[94:95], v[142:143]
	v_pk_add_f32 v[94:95], v[92:93], v[140:141]
	v_cvt_pk_bf16_f32 v92, v100, v101
	v_cvt_pk_bf16_f32 v93, v102, v103
	v_cvt_pk_bf16_f32 v94, v94, v95
	v_cvt_pk_bf16_f32 v95, v108, v109
	global_store_dwordx4 v[120:121], v[92:95], off offset:256
	v_pk_add_f32 v[96:97], v[96:97], v[132:133]
	v_pk_add_f32 v[84:85], v[84:85], v[146:147]
	v_or_b32_e32 v92, 32, v174
	v_mad_i64_i32 v[92:93], s[2:3], v92, s15, v[158:159]
	v_lshl_add_u64 v[100:101], v[92:93], 0, v[160:161]
	v_pk_add_f32 v[94:95], v[106:107], v[138:139]
	v_pk_add_f32 v[92:93], v[104:105], v[136:137]
	v_pk_add_f32 v[82:83], v[82:83], v[144:145]
	v_cvt_pk_bf16_f32 v92, v92, v93
	v_cvt_pk_bf16_f32 v93, v94, v95
	v_cvt_pk_bf16_f32 v94, v96, v97
	v_cvt_pk_bf16_f32 v95, v98, v99
	global_store_dwordx4 v[100:101], v[92:95], off
	v_pk_add_f32 v[80:81], v[80:81], v[134:135]
	v_pk_add_f32 v[78:79], v[78:79], v[132:133]
	v_pk_add_f32 v[92:93], v[76:77], v[142:143]
	v_pk_add_f32 v[76:77], v[74:75], v[140:141]
	v_cvt_pk_bf16_f32 v74, v82, v83
	v_cvt_pk_bf16_f32 v75, v84, v85
	v_cvt_pk_bf16_f32 v76, v76, v77
	v_cvt_pk_bf16_f32 v77, v92, v93
	global_store_dwordx4 v[100:101], v[74:77], off offset:256
	v_pk_add_f32 v[72:73], v[72:73], v[146:147]
	v_pk_add_f32 v[70:71], v[70:71], v[144:145]
	v_or_b32_e32 v74, 48, v174
	v_mad_i64_i32 v[74:75], s[2:3], v74, s15, v[158:159]
	v_lshl_add_u64 v[82:83], v[74:75], 0, v[160:161]
	v_pk_add_f32 v[76:77], v[88:89], v[138:139]
	v_pk_add_f32 v[74:75], v[86:87], v[136:137]
	v_pk_add_f32 v[64:65], v[64:65], v[138:139]
; DI unsigned pk2(float a, float b) { f32x2 v = {a, b}; bf16x2_t r = __builtin_convertvector(v, bf16x2_t); return __builtin_bit_cast(unsigned, r); }
; #define PG8_BAR __builtin_amdgcn_s_barrier()
; template <class Epi, class Sched, bool ALIGN_EPI = true, bool SP2 = true>
; __device__ __forceinline__ void gemm_phase(LAS unsigned char* lds, const Dims g, const Sched& S, const Epi& E) {
;     ...
;         if constexpr (ALIGN_EPI) { if (wr == 0) PG8_BAR; }
;         E(acc, cur, wr, wc, fr, fq);
;         if (!has_next) break;
; #pragma unroll
;         for (int a = 0; a < 2; ++a)
; #pragma unroll
;             for (int b = 0; b < 2; ++b)
; #pragma unroll
;                 for (int m = 0; m < 4; ++m)
; #pragma unroll
;                     for (int n = 0; n < 2; ++n) acc[a][b][m][n] = (f32x4){0.f, 0.f, 0.f, 0.f};
;         cur = nxt; cA = nA; cB = nB; ++ui;
;         if constexpr (ALIGN_EPI) { if (wr == 1) PG8_BAR; }
;     }
;     DI void operator()(const f32x4 (&acc)[2][2][4][2], const Unit& u, int wr, int wc, int fr, int fq) const {
;     ...
; #pragma unroll
;         for (int ai = 0; ai < 2; ++ai)
; #pragma unroll
;             for (int m = 0; m < 4; ++m) { bf16* rowp = O + (size_t)(row0 + ai * HALF + m * 16) * ldc + col0;
; #pragma unroll
;                 for (int bj = 0; bj < 2; ++bj) { const f32x4 v0 = acc[ai][bj][m][0] + bv[bj][0], v1 = acc[ai][bj][m][1] + bv[bj][1];
;                     u32x4 w; w.x = pk2(v0[0], v0[1]); w.y = pk2(v0[2], v0[3]); w.z = pk2(v1[0], v1[1]); w.w = pk2(v1[2], v1[3]);
;                     *(u32x4*)(rowp + bj * HALF) = w; } }
	v_cvt_pk_bf16_f32 v74, v74, v75
	v_cvt_pk_bf16_f32 v75, v76, v77
	v_cvt_pk_bf16_f32 v76, v78, v79
	v_cvt_pk_bf16_f32 v77, v80, v81
	global_store_dwordx4 v[82:83], v[74:77], off
	v_pk_add_f32 v[62:63], v[62:63], v[136:137]
	v_pk_add_f32 v[52:53], v[52:53], v[146:147]
	v_pk_add_f32 v[74:75], v[68:69], v[142:143]
	v_pk_add_f32 v[68:69], v[66:67], v[140:141]
	v_cvt_pk_bf16_f32 v66, v70, v71
	v_cvt_pk_bf16_f32 v67, v72, v73
	v_cvt_pk_bf16_f32 v68, v68, v69
	v_cvt_pk_bf16_f32 v69, v74, v75
	global_store_dwordx4 v[82:83], v[66:69], off offset:256
	v_pk_add_f32 v[50:51], v[50:51], v[144:145]
	v_pk_add_f32 v[48:49], v[48:49], v[134:135]
	v_add_u32_e32 v66, 0x80, v174
	v_mad_i64_i32 v[66:67], s[2:3], v66, s15, v[158:159]
	v_pk_add_f32 v[68:69], v[60:61], v[134:135]
	v_pk_add_f32 v[60:61], v[58:59], v[132:133]
	v_lshl_add_u64 v[66:67], v[66:67], 0, v[160:161]
	v_cvt_pk_bf16_f32 v58, v62, v63
	v_cvt_pk_bf16_f32 v59, v64, v65
	v_cvt_pk_bf16_f32 v60, v60, v61
	v_cvt_pk_bf16_f32 v61, v68, v69
	global_store_dwordx4 v[66:67], v[58:61], off
	v_pk_add_f32 v[46:47], v[46:47], v[132:133]
	v_pk_add_f32 v[36:37], v[36:37], v[146:147]
	v_pk_add_f32 v[58:59], v[44:45], v[142:143]
	v_pk_add_f32 v[44:45], v[42:43], v[140:141]
	v_cvt_pk_bf16_f32 v42, v50, v51
	v_cvt_pk_bf16_f32 v43, v52, v53
	v_cvt_pk_bf16_f32 v44, v44, v45
	v_cvt_pk_bf16_f32 v45, v58, v59
	global_store_dwordx4 v[66:67], v[42:45], off offset:256
	v_pk_add_f32 v[34:35], v[34:35], v[144:145]
	v_pk_add_f32 v[32:33], v[32:33], v[134:135]
	v_add_u32_e32 v42, 0x90, v174
	v_mad_i64_i32 v[42:43], s[2:3], v42, s15, v[158:159]
	v_lshl_add_u64 v[50:51], v[42:43], 0, v[160:161]
	v_pk_add_f32 v[44:45], v[56:57], v[138:139]
	v_pk_add_f32 v[42:43], v[54:55], v[136:137]
	v_pk_add_f32 v[30:31], v[30:31], v[132:133]
	v_cvt_pk_bf16_f32 v42, v42, v43
	v_cvt_pk_bf16_f32 v43, v44, v45
	v_cvt_pk_bf16_f32 v44, v46, v47
	v_cvt_pk_bf16_f32 v45, v48, v49
	global_store_dwordx4 v[50:51], v[42:45], off
	v_pk_add_f32 v[20:21], v[20:21], v[146:147]
	v_pk_add_f32 v[18:19], v[18:19], v[144:145]
	v_pk_add_f32 v[42:43], v[28:29], v[142:143]
	v_pk_add_f32 v[28:29], v[26:27], v[140:141]
	v_cvt_pk_bf16_f32 v26, v34, v35
	v_cvt_pk_bf16_f32 v27, v36, v37
	v_cvt_pk_bf16_f32 v28, v28, v29
	v_cvt_pk_bf16_f32 v29, v42, v43
	global_store_dwordx4 v[50:51], v[26:29], off offset:256
	v_pk_add_f32 v[16:17], v[16:17], v[134:135]
	v_pk_add_f32 v[14:15], v[14:15], v[132:133]
	v_add_u32_e32 v26, 0xa0, v174
	v_mad_i64_i32 v[26:27], s[2:3], v26, s15, v[158:159]
	v_lshl_add_u64 v[34:35], v[26:27], 0, v[160:161]
	v_pk_add_f32 v[28:29], v[40:41], v[138:139]
	v_pk_add_f32 v[26:27], v[38:39], v[136:137]
	v_pk_add_f32 v[8:9], v[8:9], v[146:147]
	v_cvt_pk_bf16_f32 v26, v26, v27
	v_cvt_pk_bf16_f32 v27, v28, v29
	v_cvt_pk_bf16_f32 v28, v30, v31
	v_cvt_pk_bf16_f32 v29, v32, v33
	global_store_dwordx4 v[34:35], v[26:29], off
	v_pk_add_f32 v[6:7], v[6:7], v[144:145]
	s_andn2_b64 vcc, exec, s[38:39]
	v_pk_add_f32 v[26:27], v[12:13], v[142:143]
	v_pk_add_f32 v[12:13], v[10:11], v[140:141]
	v_cvt_pk_bf16_f32 v10, v18, v19
	v_cvt_pk_bf16_f32 v11, v20, v21
	v_cvt_pk_bf16_f32 v12, v12, v13
	v_cvt_pk_bf16_f32 v13, v26, v27
	global_store_dwordx4 v[34:35], v[10:13], off offset:256
	s_nop 1
	v_add_u32_e32 v10, 0xb0, v174
	v_mad_i64_i32 v[10:11], s[2:3], v10, s15, v[158:159]
	v_lshl_add_u64 v[18:19], v[10:11], 0, v[160:161]
	v_pk_add_f32 v[12:13], v[24:25], v[138:139]
	v_pk_add_f32 v[10:11], v[22:23], v[136:137]
	s_mov_b64 s[2:3], -1
	v_cvt_pk_bf16_f32 v10, v10, v11
	v_cvt_pk_bf16_f32 v11, v12, v13
	v_cvt_pk_bf16_f32 v12, v14, v15
	v_cvt_pk_bf16_f32 v13, v16, v17
	global_store_dwordx4 v[18:19], v[10:13], off
	s_nop 1
	v_pk_add_f32 v[10:11], v[4:5], v[142:143]
	v_pk_add_f32 v[4:5], v[2:3], v[140:141]
	v_cvt_pk_bf16_f32 v2, v6, v7
	v_cvt_pk_bf16_f32 v3, v8, v9
	v_cvt_pk_bf16_f32 v4, v4, v5
	v_cvt_pk_bf16_f32 v5, v10, v11
	global_store_dwordx4 v[18:19], v[2:5], off offset:256
	s_cbranch_vccnz .LBB0_318
	s_andn2_b64 vcc, exec, s[8:9]
	s_cbranch_vccnz .LBB0_317
	s_barrier
	s_branch .LBB0_317
